# diff-combine phase: the 16 loads of a row issued together into 16 registers with one wait (hipcc had serialized them into four load/wait groups reusing four registers)
# speedup vs baseline: 1.0083x; 1.0083x over previous
; __device__ __forceinline__ bf16_t f2bf(float f) { unsigned u = __float_as_uint(f); return (bf16_t)((u + 0x7fffu + ((u >> 16) & 1u)) >> 16); }
; __host__ __device__ inline float lam_init_of(int l) { return 0.8f - 0.6f * expf(-0.3f * (float)l); }
; __device__ __forceinline__ void ph_diffc(const P& p, int l, int row0, int gw, int nw, int lane) {
;   const float lam = WSP(float, WS_SMALL)[1024 + l], li = lam_init_of(l);
;   const float d0 = p.dn[l * 128 + lane] * (1.f - li), d1 = p.dn[l * 128 + lane + 64] * (1.f - li);
;   for (int t = row0 + gw; t < NTOK; t += nw) {
;     const float* d = WSP(float, WS_DTMP) + (size_t)t * 1024;
;     float a[4], b[4];
; #pragma unroll
;     for (int h = 0; h < 4; ++h) { const float x0 = d[h * 256 + lane], x1 = d[h * 256 + 128 + lane], y0 = d[h * 256 + 64 + lane], y1 = d[h * 256 + 192 + lane]; a[h] = x0 - lam * x1; b[h] = y0 - lam * y1; }
;     bf16_t* m = WSP(bf16_t, WS_MIX) + (size_t)t * DM + 1536;
; #pragma unroll
;     for (int h = 0; h < 4; ++h) { const float rs = rsqrtf(wave_sum(a[h] * a[h] + b[h] * b[h]) * (1.f / 128) + EPS);
;       m[h * 128 + lane] = f2bf(a[h] * rs * d0); m[h * 128 + lane + 64] = f2bf(b[h] * rs * d1); }
;   }
; }
.LBB0_568:
	v_lshl_add_u64 v[18:19], s[22:23], 0, v[6:7]
	v_add_co_u32_e32 v18, vcc, 0x2f914000, v18
	v_lshl_add_u64 v[24:25], s[22:23], 0, v[8:9]
	s_nop 0
	v_addc_co_u32_e32 v19, vcc, 0, v19, vcc
	global_load_dword v20, v[18:19], off
	global_load_dword v21, v[18:19], off offset:512
	global_load_dword v22, v[18:19], off offset:256
	global_load_dword v23, v[18:19], off offset:768
	global_load_dword v100, v[18:19], off offset:1024
	global_load_dword v101, v[18:19], off offset:1536
	global_load_dword v102, v[18:19], off offset:1280
	global_load_dword v103, v[18:19], off offset:1792
	global_load_dword v104, v[18:19], off offset:2048
	global_load_dword v105, v[18:19], off offset:2560
	global_load_dword v106, v[18:19], off offset:2304
	global_load_dword v107, v[18:19], off offset:2816
	global_load_dword v108, v[18:19], off offset:3072
	global_load_dword v109, v[18:19], off offset:3584
	global_load_dword v110, v[18:19], off offset:3328
	s_nop 0
	global_load_dword v18, v[18:19], off offset:3840
	s_waitcnt vmcnt(0)
	s_add_i32 s14, s14, s18
	v_fma_f32 v26, -v15, v21, v20
	v_fma_f32 v27, -v15, v23, v22
	v_fma_f32 v28, -v15, v101, v100
	v_fma_f32 v29, -v15, v103, v102
	v_fma_f32 v30, -v15, v105, v104
	v_fma_f32 v31, -v15, v107, v106
	v_fma_f32 v19, -v15, v109, v108
	v_mul_f32_e32 v20, v27, v27
	v_fmac_f32_e32 v20, v26, v26
	v_fma_f32 v18, -v15, v18, v110
	v_add_f32_dpp v20, v20, v20 quad_perm:[1,0,3,2] row_mask:0xf bank_mask:0xf bound_ctrl:1
	s_nop 1
	v_add_f32_dpp v20, v20, v20 quad_perm:[2,3,0,1] row_mask:0xf bank_mask:0xf bound_ctrl:1
	s_nop 1
	v_add_f32_dpp v20, v20, v20 row_half_mirror row_mask:0xf bank_mask:0xf bound_ctrl:1
	s_nop 1
	v_add_f32_dpp v20, v20, v20 row_mirror row_mask:0xf bank_mask:0xf bound_ctrl:1
	v_mov_b32_e32 v21, v20
	s_nop 1
	v_permlane16_swap_b32_e32 v20, v21
	v_add_f32_e32 v21, v20, v21
	v_mul_f32_e32 v20, v29, v29
	v_fmac_f32_e32 v20, v28, v28
	v_mov_b32_e32 v23, v21
	s_nop 1
	v_permlane32_swap_b32_e32 v21, v23
	v_add_f32_dpp v20, v20, v20 quad_perm:[1,0,3,2] row_mask:0xf bank_mask:0xf bound_ctrl:1
	s_nop 1
	v_add_f32_dpp v20, v20, v20 quad_perm:[2,3,0,1] row_mask:0xf bank_mask:0xf bound_ctrl:1
	s_nop 1
	v_add_f32_dpp v20, v20, v20 row_half_mirror row_mask:0xf bank_mask:0xf bound_ctrl:1
	s_nop 1
	v_add_f32_dpp v20, v20, v20 row_mirror row_mask:0xf bank_mask:0xf bound_ctrl:1
	v_mov_b32_e32 v22, v20
	s_nop 1
	v_permlane16_swap_b32_e32 v20, v22
	v_add_f32_e32 v20, v20, v22
	v_mov_b32_e32 v22, v20
	s_nop 1
	v_permlane32_swap_b32_e32 v20, v22
	v_pk_add_f32 v[20:21], v[20:21], v[22:23]
	v_mov_b64_e32 v[22:23], s[16:17]
	v_pk_fma_f32 v[20:21], v[20:21], s[6:7], v[22:23] op_sel_hi:[1,0,0]
	s_nop 0
	v_mul_f32_e32 v32, 0x4b800000, v21
	v_cmp_gt_f32_e64 s[40:41], s37, v21
	v_cmp_gt_f32_e32 vcc, s37, v20
	s_nop 0
	v_cndmask_b32_e64 v21, v21, v32, s[40:41]
	v_rsq_f32_e32 v21, v21
	s_nop 0
	v_mul_f32_e32 v32, 0x45800000, v21
	v_cndmask_b32_e64 v21, v21, v32, s[40:41]
	v_mul_f32_e32 v26, v26, v21
	v_mul_f32_e32 v26, v16, v26
	v_bfe_u32 v32, v26, 16, 1
	v_add_co_u32_e64 v24, s[40:41], s2, v24
	v_mul_f32_e32 v21, v27, v21
	v_add3_u32 v26, v26, v32, s86
	v_addc_co_u32_e64 v25, s[40:41], 0, v25, s[40:41]
	v_mul_f32_e32 v21, v17, v21
	global_store_short_d16_hi v[24:25], v26, off offset:3072
	v_bfe_u32 v26, v21, 16, 1
	v_add3_u32 v21, v21, v26, s86
	global_store_short_d16_hi v[24:25], v21, off offset:3200
	v_mul_f32_e32 v21, 0x4b800000, v20
	v_cndmask_b32_e32 v20, v20, v21, vcc
	v_rsq_f32_e32 v20, v20
	s_nop 0
	v_mul_f32_e32 v21, 0x45800000, v20
	v_cndmask_b32_e32 v26, v20, v21, vcc
	v_mul_f32_e32 v20, v28, v26
	v_mul_f32_e32 v20, v16, v20
	v_bfe_u32 v21, v20, 16, 1
	v_add3_u32 v27, v20, v21, s86
	v_lshl_add_u64 v[20:21], s[22:23], 0, v[10:11]
	v_add_co_u32_e32 v20, vcc, s2, v20
	v_mul_f32_e32 v26, v29, v26
	s_nop 0
	v_addc_co_u32_e32 v21, vcc, 0, v21, vcc
	v_mul_f32_e32 v26, v17, v26
	global_store_short_d16_hi v[20:21], v27, off offset:3072
	v_bfe_u32 v27, v26, 16, 1
	v_add3_u32 v26, v26, v27, s86
	global_store_short_d16_hi v[20:21], v26, off offset:3200
	v_mul_f32_e32 v20, v31, v31
	v_fmac_f32_e32 v20, v30, v30
	s_nop 1
	v_add_f32_dpp v20, v20, v20 quad_perm:[1,0,3,2] row_mask:0xf bank_mask:0xf bound_ctrl:1
	s_nop 1
	v_add_f32_dpp v20, v20, v20 quad_perm:[2,3,0,1] row_mask:0xf bank_mask:0xf bound_ctrl:1
	s_nop 1
	v_add_f32_dpp v20, v20, v20 row_half_mirror row_mask:0xf bank_mask:0xf bound_ctrl:1
	s_nop 1
	v_add_f32_dpp v20, v20, v20 row_mirror row_mask:0xf bank_mask:0xf bound_ctrl:1
	v_mov_b32_e32 v21, v20
	s_nop 1
	v_permlane16_swap_b32_e32 v20, v21
	v_add_f32_e32 v21, v20, v21
	v_mul_f32_e32 v20, v18, v18
	v_fmac_f32_e32 v20, v19, v19
	v_mov_b32_e32 v27, v21
	s_nop 1
	v_permlane32_swap_b32_e32 v21, v27
	v_add_f32_dpp v20, v20, v20 quad_perm:[1,0,3,2] row_mask:0xf bank_mask:0xf bound_ctrl:1
	s_nop 1
	v_add_f32_dpp v20, v20, v20 quad_perm:[2,3,0,1] row_mask:0xf bank_mask:0xf bound_ctrl:1
	s_nop 1
	v_add_f32_dpp v20, v20, v20 row_half_mirror row_mask:0xf bank_mask:0xf bound_ctrl:1
	s_nop 1
	v_add_f32_dpp v20, v20, v20 row_mirror row_mask:0xf bank_mask:0xf bound_ctrl:1
	v_mov_b32_e32 v26, v20
	s_nop 1
	v_permlane16_swap_b32_e32 v20, v26
	v_add_f32_e32 v20, v20, v26
	v_mov_b32_e32 v26, v20
	s_nop 1
	v_permlane32_swap_b32_e32 v20, v26
	v_pk_add_f32 v[20:21], v[20:21], v[26:27]
	s_nop 0
	v_pk_fma_f32 v[20:21], v[20:21], s[6:7], v[22:23] op_sel_hi:[1,0,0]
	s_nop 0
	v_mul_f32_e32 v22, 0x4b800000, v21
	v_cmp_gt_f32_e64 s[40:41], s37, v21
	v_cmp_gt_f32_e32 vcc, s37, v20
	s_nop 0
	v_cndmask_b32_e64 v21, v21, v22, s[40:41]
	v_rsq_f32_e32 v21, v21
	s_nop 0
	v_mul_f32_e32 v22, 0x45800000, v21
	v_cndmask_b32_e64 v21, v21, v22, s[40:41]
	v_mul_f32_e32 v22, v30, v21
	v_mul_f32_e32 v22, v16, v22
	v_bfe_u32 v23, v22, 16, 1
	v_mul_f32_e32 v21, v31, v21
	v_add3_u32 v22, v22, v23, s86
	v_mul_f32_e32 v21, v17, v21
	global_store_short_d16_hi v[24:25], v22, off offset:3584
	v_bfe_u32 v22, v21, 16, 1
	v_add3_u32 v21, v21, v22, s86
	global_store_short_d16_hi v[24:25], v21, off offset:3712
	v_mul_f32_e32 v21, 0x4b800000, v20
	v_cndmask_b32_e32 v20, v20, v21, vcc
	v_rsq_f32_e32 v20, v20
	s_nop 0
	v_mul_f32_e32 v21, 0x45800000, v20
	v_cndmask_b32_e32 v22, v20, v21, vcc
	v_mul_f32_e32 v19, v19, v22
	v_mul_f32_e32 v19, v16, v19
	v_bfe_u32 v20, v19, 16, 1
	v_add3_u32 v19, v19, v20, s86
	v_lshl_add_u64 v[20:21], s[22:23], 0, v[12:13]
	v_add_co_u32_e32 v20, vcc, s2, v20
	v_mul_f32_e32 v18, v18, v22
	s_nop 0
	v_addc_co_u32_e32 v21, vcc, 0, v21, vcc
	v_mul_f32_e32 v18, v17, v18
	s_add_u32 s22, s22, s34
	global_store_short_d16_hi v[20:21], v19, off offset:3072
	v_bfe_u32 v19, v18, 16, 1
	s_addc_u32 s23, s23, s35
	v_add3_u32 v18, v18, v19, s86
	s_cmpk_lt_i32 s14, 0x2100
	global_store_short_d16_hi v[20:21], v18, off offset:3200
	s_cbranch_scc1 .LBB0_568

; __device__ __forceinline__ bf16_t f2bf(float f) { unsigned u = __float_as_uint(f); return (bf16_t)((u + 0x7fffu + ((u >> 16) & 1u)) >> 16); }
; __host__ __device__ inline float lam_init_of(int l) { return 0.8f - 0.6f * expf(-0.3f * (float)l); }
; __device__ __forceinline__ void ph_diffc(const P& p, int l, int row0, int gw, int nw, int lane) {
;   const float lam = WSP(float, WS_SMALL)[1024 + l], li = lam_init_of(l);
;   const float d0 = p.dn[l * 128 + lane] * (1.f - li), d1 = p.dn[l * 128 + lane + 64] * (1.f - li);
;   for (int t = row0 + gw; t < NTOK; t += nw) {
;     const float* d = WSP(float, WS_DTMP) + (size_t)t * 1024;
;     float a[4], b[4];
; #pragma unroll
;     for (int h = 0; h < 4; ++h) { const float x0 = d[h * 256 + lane], x1 = d[h * 256 + 128 + lane], y0 = d[h * 256 + 64 + lane], y1 = d[h * 256 + 192 + lane]; a[h] = x0 - lam * x1; b[h] = y0 - lam * y1; }
;     bf16_t* m = WSP(bf16_t, WS_MIX) + (size_t)t * DM + 1536;
; #pragma unroll
;     for (int h = 0; h < 4; ++h) { const float rs = rsqrtf(wave_sum(a[h] * a[h] + b[h] * b[h]) * (1.f / 128) + EPS);
;       m[h * 128 + lane] = f2bf(a[h] * rs * d0); m[h * 128 + lane + 64] = f2bf(b[h] * rs * d1); }
;   }
; }
.LBB0_592:
	v_lshl_add_u64 v[12:13], s[12:13], 0, v[4:5]
	v_add_co_u32_e32 v12, vcc, 0x2f914000, v12
	s_add_i32 s14, s14, s0
	s_nop 0
	v_addc_co_u32_e32 v13, vcc, 0, v13, vcc
	global_load_dword v11, v[12:13], off
	global_load_dword v14, v[12:13], off offset:512
	global_load_dword v15, v[12:13], off offset:256
	global_load_dword v16, v[12:13], off offset:768
	global_load_dword v100, v[12:13], off offset:1024
	global_load_dword v101, v[12:13], off offset:1536
	global_load_dword v102, v[12:13], off offset:1280
	global_load_dword v103, v[12:13], off offset:1792
	global_load_dword v104, v[12:13], off offset:2048
	global_load_dword v105, v[12:13], off offset:2560
	global_load_dword v106, v[12:13], off offset:2304
	global_load_dword v107, v[12:13], off offset:2816
	global_load_dword v108, v[12:13], off offset:3072
	global_load_dword v109, v[12:13], off offset:3584
	global_load_dword v110, v[12:13], off offset:3328
	s_nop 0
	global_load_dword v12, v[12:13], off offset:3840
	s_waitcnt vmcnt(0)
	v_fma_f32 v18, -v8, v14, v11
	v_fma_f32 v19, -v8, v16, v15
	v_fma_f32 v20, -v8, v101, v100
	v_fma_f32 v21, -v8, v103, v102
	v_fma_f32 v22, -v8, v105, v104
	v_fma_f32 v23, -v8, v107, v106
	v_lshl_add_u64 v[16:17], s[12:13], 0, v[6:7]
	v_fma_f32 v24, -v8, v109, v108
	v_fma_f32 v11, -v8, v12, v110
	v_mul_f32_e32 v12, v19, v19
	v_fmac_f32_e32 v12, v18, v18
	s_nop 1
	v_add_f32_dpp v12, v12, v12 quad_perm:[1,0,3,2] row_mask:0xf bank_mask:0xf bound_ctrl:1
	s_nop 1
	v_add_f32_dpp v12, v12, v12 quad_perm:[2,3,0,1] row_mask:0xf bank_mask:0xf bound_ctrl:1
	s_nop 1
	v_add_f32_dpp v12, v12, v12 row_half_mirror row_mask:0xf bank_mask:0xf bound_ctrl:1
	s_nop 1
	v_add_f32_dpp v12, v12, v12 row_mirror row_mask:0xf bank_mask:0xf bound_ctrl:1
	v_mov_b32_e32 v13, v12
	s_nop 1
	v_permlane16_swap_b32_e32 v12, v13
	v_add_f32_e32 v13, v12, v13
	v_mul_f32_e32 v12, v21, v21
	v_fmac_f32_e32 v12, v20, v20
	v_mov_b32_e32 v15, v13
	s_nop 1
	v_permlane32_swap_b32_e32 v13, v15
	v_add_f32_dpp v12, v12, v12 quad_perm:[1,0,3,2] row_mask:0xf bank_mask:0xf bound_ctrl:1
	s_nop 1
	v_add_f32_dpp v12, v12, v12 quad_perm:[2,3,0,1] row_mask:0xf bank_mask:0xf bound_ctrl:1
	s_nop 1
	v_add_f32_dpp v12, v12, v12 row_half_mirror row_mask:0xf bank_mask:0xf bound_ctrl:1
	s_nop 1
	v_add_f32_dpp v12, v12, v12 row_mirror row_mask:0xf bank_mask:0xf bound_ctrl:1
	v_mov_b32_e32 v14, v12
	s_nop 1
	v_permlane16_swap_b32_e32 v12, v14
	v_add_f32_e32 v12, v12, v14
	v_mov_b32_e32 v14, v12
	s_nop 1
	v_permlane32_swap_b32_e32 v12, v14
	v_pk_add_f32 v[12:13], v[12:13], v[14:15]
	v_mov_b64_e32 v[14:15], s[4:5]
	v_pk_fma_f32 v[12:13], v[12:13], s[2:3], v[14:15] op_sel_hi:[1,0,0]
	s_nop 0
	v_mul_f32_e32 v25, 0x4b800000, v13
	v_cmp_gt_f32_e64 s[40:41], s37, v13
	v_cmp_gt_f32_e32 vcc, s37, v12
	s_nop 0
	v_cndmask_b32_e64 v13, v13, v25, s[40:41]
	v_rsq_f32_e32 v13, v13
	s_nop 0
	v_mul_f32_e32 v25, 0x45800000, v13
	v_cndmask_b32_e64 v13, v13, v25, s[40:41]
	v_mul_f32_e32 v18, v18, v13
	v_mul_f32_e32 v18, v9, v18
	v_bfe_u32 v25, v18, 16, 1
	v_add_co_u32_e64 v16, s[40:41], s1, v16
	v_mul_f32_e32 v13, v19, v13
	v_add3_u32 v18, v18, v25, s86
	v_addc_co_u32_e64 v17, s[40:41], 0, v17, s[40:41]
	v_mul_f32_e32 v13, v10, v13
	global_store_short_d16_hi v[16:17], v18, off offset:3072
	v_bfe_u32 v18, v13, 16, 1
	v_add3_u32 v13, v13, v18, s86
	global_store_short_d16_hi v[16:17], v13, off offset:3200
	v_mul_f32_e32 v13, 0x4b800000, v12
	v_cndmask_b32_e32 v12, v12, v13, vcc
	v_rsq_f32_e32 v12, v12
	s_nop 0
	v_mul_f32_e32 v13, 0x45800000, v12
	v_cndmask_b32_e32 v18, v12, v13, vcc
	v_mul_f32_e32 v12, v20, v18
	v_mul_f32_e32 v12, v9, v12
	v_bfe_u32 v13, v12, 16, 1
	v_add3_u32 v19, v12, v13, s86
	v_lshl_add_u64 v[12:13], s[12:13], 0, v[2:3]
	v_add_co_u32_e32 v12, vcc, s1, v12
	v_mul_f32_e32 v18, v21, v18
	s_nop 0
	v_addc_co_u32_e32 v13, vcc, 0, v13, vcc
	v_mul_f32_e32 v18, v10, v18
	global_store_short_d16_hi v[12:13], v19, off offset:3072
	v_bfe_u32 v19, v18, 16, 1
	v_add3_u32 v18, v18, v19, s86
	global_store_short_d16_hi v[12:13], v18, off offset:3200
	v_mul_f32_e32 v12, v23, v23
	v_fmac_f32_e32 v12, v22, v22
	s_nop 1
	v_add_f32_dpp v12, v12, v12 quad_perm:[1,0,3,2] row_mask:0xf bank_mask:0xf bound_ctrl:1
	s_nop 1
	v_add_f32_dpp v12, v12, v12 quad_perm:[2,3,0,1] row_mask:0xf bank_mask:0xf bound_ctrl:1
	s_nop 1
	v_add_f32_dpp v12, v12, v12 row_half_mirror row_mask:0xf bank_mask:0xf bound_ctrl:1
	s_nop 1
	v_add_f32_dpp v12, v12, v12 row_mirror row_mask:0xf bank_mask:0xf bound_ctrl:1
	v_mov_b32_e32 v13, v12
	s_nop 1
	v_permlane16_swap_b32_e32 v12, v13
	v_add_f32_e32 v13, v12, v13
	v_mul_f32_e32 v12, v11, v11
	v_fmac_f32_e32 v12, v24, v24
	v_mov_b32_e32 v19, v13
	s_nop 1
	v_permlane32_swap_b32_e32 v13, v19
	v_add_f32_dpp v12, v12, v12 quad_perm:[1,0,3,2] row_mask:0xf bank_mask:0xf bound_ctrl:1
	s_nop 1
	v_add_f32_dpp v12, v12, v12 quad_perm:[2,3,0,1] row_mask:0xf bank_mask:0xf bound_ctrl:1
	s_nop 1
	v_add_f32_dpp v12, v12, v12 row_half_mirror row_mask:0xf bank_mask:0xf bound_ctrl:1
	s_nop 1
	v_add_f32_dpp v12, v12, v12 row_mirror row_mask:0xf bank_mask:0xf bound_ctrl:1
	v_mov_b32_e32 v18, v12
	s_nop 1
	v_permlane16_swap_b32_e32 v12, v18
	v_add_f32_e32 v12, v12, v18
	v_mov_b32_e32 v18, v12
	s_nop 1
	v_permlane32_swap_b32_e32 v12, v18
	v_pk_add_f32 v[12:13], v[12:13], v[18:19]
	s_nop 0
	v_pk_fma_f32 v[12:13], v[12:13], s[2:3], v[14:15] op_sel_hi:[1,0,0]
	s_nop 0
	v_mul_f32_e32 v14, 0x4b800000, v13
	v_cmp_gt_f32_e64 s[40:41], s37, v13
	v_cmp_gt_f32_e32 vcc, s37, v12
	s_nop 0
	v_cndmask_b32_e64 v13, v13, v14, s[40:41]
	v_rsq_f32_e32 v13, v13
	s_nop 0
	v_mul_f32_e32 v14, 0x45800000, v13
	v_cndmask_b32_e64 v13, v13, v14, s[40:41]
	v_mul_f32_e32 v14, v22, v13
	v_mul_f32_e32 v14, v9, v14
	v_bfe_u32 v15, v14, 16, 1
	v_mul_f32_e32 v13, v23, v13
	v_add3_u32 v14, v14, v15, s86
	v_mul_f32_e32 v13, v10, v13
	global_store_short_d16_hi v[16:17], v14, off offset:3584
	v_bfe_u32 v14, v13, 16, 1
	v_add3_u32 v13, v13, v14, s86
	global_store_short_d16_hi v[16:17], v13, off offset:3712
	v_mul_f32_e32 v13, 0x4b800000, v12
	v_cndmask_b32_e32 v12, v12, v13, vcc
	v_rsq_f32_e32 v12, v12
	s_nop 0
	v_mul_f32_e32 v13, 0x45800000, v12
	v_cndmask_b32_e32 v14, v12, v13, vcc
	v_mul_f32_e32 v12, v24, v14
	v_mul_f32_e32 v12, v9, v12
	v_bfe_u32 v13, v12, 16, 1
	v_mul_f32_e32 v11, v11, v14
	v_add3_u32 v15, v12, v13, s86
	v_lshl_add_u64 v[12:13], s[12:13], 0, v[0:1]
	v_mul_f32_e32 v11, v10, v11
	s_add_u32 s12, s12, s18
	v_add_co_u32_e32 v12, vcc, s1, v12
	v_bfe_u32 v14, v11, 16, 1
	s_addc_u32 s13, s13, s19
	v_addc_co_u32_e32 v13, vcc, 0, v13, vcc
	v_add3_u32 v11, v11, v14, s86
	s_cmpk_gt_i32 s14, 0x20ff
	global_store_short_d16_hi v[12:13], v15, off offset:3072
	global_store_short_d16_hi v[12:13], v11, off offset:3200
	s_cbranch_scc0 .LBB0_592
